# v21 + LDS bank-conflict-free swizzle for the MLA K image: chunk position c ^ (r&15) (writer koff in both copies, reader mask 0xf0)
# baseline (speedup 1.0000x reference)
; #define LAS __attribute__((address_space(3)))
; __device__ __forceinline__ int v_rd_base(int lane) { return ((lane & 3) << 3) | (((lane >> 2) & 3) << 6) | (((lane >> 4) & 1) << 5) | (((lane >> 5) & 1) << 8); }
; template <int DK, int DV, bool OFF, class QLoader> ...
;     ...
;   QL.load(qr, wid * QBLK + r32, hi);
;   asm volatile("s_waitcnt vmcnt(0)" ::: "memory");
;   unsigned koff[KPW], voff[VPW];
; #pragma unroll
;   for (int i = 0; i < (DK == 64 ? 1 : KPW); ++i) { const int row = (wid * KPW + i) * 4 + (lane >> 4); int c = (lane & 15) ^ (row & 7); c = (c < DK / 8) ? c : (c & 7); koff[i] = (unsigned)((row * ldk) * 2 + c * 16); }
; #pragma unroll
;   for (int i = 0; i < 1; ++i) { const int sidx = (wid * VPW + i) * 2 + (lane >> 5), kg = sidx / ND, st = sidx % ND, kk = kg * 8 + ((lane & 31) >> 2);
;     const int k = (kk & ~0xC) | ((kk & 4) << 1) | ((kk & 8) >> 1), c = st * 32 + (lane & 3) * 8; voff[i] = (unsigned)((k * ldv + c) * 2); }
;   const int vb0 = (int)(uintptr_t)V_lds + v_rd_base(lane);
;   LAS unsigned* const ldsK = (LAS unsigned*)(LAS char*)K_lds + (wid * KPW) * 256; LAS unsigned* const ldsV = (LAS unsigned*)(LAS char*)V_lds + (wid * VPW) * 256;
; __device__ __forceinline__ void mla_attn_phase(Frame& F, const InPtrs& A, int jl, bool do_ctx, int conv_layer) {
;     ...
;         const bool lat = u < 2048; const int bh = lat ? (u >> 4) : (u - 2048), qb = lat ? (u & 15) : 0, b = bh >> 4, h = bh & 15;
;         const int row0 = lat ? b * 4096 + qb * 256 : NLAT + b * 256;
;         const att::QLoadMLA QL{QPRE + (size_t)row0 * 1536 + h * 96, RQ + row0, gq, lat ? ropeA + (size_t)(qb * 256) * 16 : nullptr};
;         const bf16* Kp = MK + (size_t)bh * NKEYS * 96; const bf16* Vp = MV + (size_t)bh * NKEYS * 64;
;         bf16* Op = AO + (size_t)row0 * 1024 + h * 64;
.LBB0_1412:
	s_and_b32 s30, s22, 15
	s_ashr_i32 s1, s0, 31
	s_mul_i32 s17, s0, 0xc00
	s_mul_hi_i32 s16, s0, 0xc00
	s_add_u32 s17, s63, s17
	s_addc_u32 s16, s64, s16
	s_mul_i32 s20, s30, 0xc0
	s_add_u32 s28, s17, s20
	s_addc_u32 s29, s16, 0
	s_lshl_b64 s[16:17], s[0:1], 2
	s_add_u32 s26, s72, s16
	s_addc_u32 s27, s73, s17
	s_lshl_b32 s2, s2, 14
	s_add_u32 s24, s69, s2
	s_addc_u32 s25, s70, 0
	s_mul_i32 s78, s22, 0xcc000
	s_mul_hi_i32 s2, s22, 0xcc000
	s_add_u32 s20, s65, s78
	s_addc_u32 s21, s66, s2
	s_mul_i32 s80, s22, 0x88000
	s_mul_hi_i32 s79, s22, 0x88000
	s_add_u32 s22, s74, s80
	s_addc_u32 s23, s75, s79
	s_lshl_b64 s[0:1], s[0:1], 11
	s_add_u32 s0, s67, s0
	s_addc_u32 s1, s68, s1
	s_lshl_b32 s16, s30, 7
	s_add_u32 s16, s0, s16
	v_cndmask_b32_e64 v0, 0, 1, s[18:19]
	s_addc_u32 s17, s1, 0
	s_mov_b64 s[0:1], -1
	s_andn2_b64 vcc, exec, s[34:35]
	v_cmp_ne_u32_e64 s[36:37], 1, v0
	s_cbranch_vccnz .LBB0_1463
	v_mov_b32_e32 v56, v180
	v_mov_b64_e32 v[2:3], s[28:29]
	v_readfirstlane_b32 s31, v56
	s_ashr_i32 s38, s31, 6
	v_and_b32_e32 v55, 31, v56
	s_lshl_b32 s30, s38, 5
	v_bfe_u32 v57, v56, 5, 1
	v_or_b32_e32 v36, s30, v55
	s_movk_i32 s0, 0xc00
	v_mad_i64_i32 v[2:3], s[0:1], v36, s0, v[2:3]
	v_lshlrev_b32_e32 v34, 4, v57
	v_mov_b32_e32 v35, v1
	v_lshl_add_u64 v[2:3], v[2:3], 0, v[34:35]
	v_bfe_u32 v188, v56, 4, 2
	v_lshl_or_b32 v189, s38, 3, v188
	v_bitop3_b32 v193, v188, v56, 15 bitop3:0x78
	s_and_b32 s39, s38, 1
	s_lshl_b32 s39, s39, 3
	v_xor_b32_e32 v193, s39, v193
	s_movk_i32 s0, 0xc0
	v_and_b32_e32 v192, 15, v56
	v_mul_lo_u32 v194, v189, s0
	v_lshlrev_b32_e32 v189, 4, v193
	v_and_b32_e32 v193, 0x70, v189
	v_cmp_gt_u32_e32 vcc, 0xc0, v189
	v_bitop3_b32 v192, v188, v192, 4 bitop3:0x36
	v_xor_b32_e32 v192, s39, v192
	v_lshl_or_b32 v199, s38, 1, v57
	v_cndmask_b32_e32 v197, v193, v189, vcc
	v_lshlrev_b32_e32 v193, 4, v192
	v_cmp_gt_u32_e32 vcc, 12, v192
	v_lshrrev_b32_e32 v192, 31, v199
	v_and_b32_e32 v195, 0x70, v193
	v_add_u32_e32 v192, v199, v192
	v_cndmask_b32_e32 v196, v195, v193, vcc
	s_movk_i32 s0, 0x300
	v_ashrrev_i32_e32 v198, 1, v192
	v_add_u32_e32 v189, v197, v194
	v_add3_u32 v204, v194, v196, s0
	v_lshlrev_b32_e32 v193, 3, v198
	v_lshrrev_b32_e32 v194, 2, v55
	s_mov_b32 s0, 0x1fffff3
	v_bitop3_b32 v200, v193, s0, v194 bitop3:0xc8
	s_lshl_b32 s0, s38, 11
	v_lshrrev_b32_e32 v193, 1, v55
	s_add_i32 s87, s0, 0
	v_and_b32_e32 v192, 0x3fffffe, v192
	v_and_b32_e32 v201, 8, v193
	v_lshlrev_b32_e32 v193, 2, v198
	v_lshlrev_b32_e32 v194, 4, v56
	s_add_i32 s81, s87, 0x8000
	s_lshl_b32 s1, s38, 10
	v_sub_u32_e32 v192, v199, v192
	v_and_b32_e32 v202, 4, v193
	v_and_b32_e32 v203, 48, v194
	s_sub_i32 s0, 0, s1
	s_sub_i32 s1, s87, s1
	s_mov_b32 m0, s81
	s_add_i32 s82, s87, 0x8400
	v_or3_b32 v193, v201, v200, v202
	v_lshl_or_b32 v192, v192, 6, v203
	global_load_lds_dwordx4 v189, s[20:21]
	s_mov_b32 m0, s82
	s_add_u32 s40, s20, 0x3000
	v_lshl_add_u32 v192, v193, 7, v192
	global_load_lds_dwordx4 v204, s[20:21]
	s_mov_b32 m0, s1
	s_addc_u32 s41, s21, 0
	s_add_i32 s83, s87, 0xc000
	global_load_lds_dwordx4 v192, s[22:23]
	s_mov_b32 m0, s83
	s_add_i32 s84, s87, 0xc400
	v_mov_b32_e32 v193, v1
	global_load_lds_dwordx4 v189, s[40:41]
	s_mov_b32 m0, s84
	v_lshl_add_u64 v[206:207], s[22:23], 0, v[192:193]
	global_load_lds_dwordx4 v204, s[40:41]
	s_mov_b64 s[40:41], 0x2000
	s_add_i32 m0, s1, 0x2000
	v_lshl_add_u64 v[192:193], v[206:207], 0, s[40:41]
	s_add_u32 s40, s20, 0x6000
	global_load_lds_dwordx4 v[192:193], off
	global_load_dwordx4 v[38:41], v[2:3], off
	global_load_dwordx4 v[42:45], v[2:3], off offset:32
	global_load_dwordx4 v[46:49], v[2:3], off offset:64
	global_load_dwordx4 v[50:53], v[2:3], off offset:96
	v_ashrrev_i32_e32 v37, 31, v36
	v_lshl_add_u64 v[4:5], v[36:37], 2, s[26:27]
	global_load_dword v0, v[4:5], off
	global_load_dwordx4 v[90:93], v[2:3], off offset:128
	global_load_dwordx4 v[94:97], v[2:3], off offset:160
	v_and_b32_e32 v35, 32, v56
	global_load_dwordx4 v[6:9], v35, s[14:15] offset:16
	global_load_dwordx4 v[2:5], v35, s[14:15]
	global_load_dwordx4 v[14:17], v35, s[14:15] offset:80
	global_load_dwordx4 v[10:13], v35, s[14:15] offset:64
	global_load_dwordx4 v[22:25], v35, s[14:15] offset:144
	global_load_dwordx4 v[18:21], v35, s[14:15] offset:128
	global_load_dwordx4 v[30:33], v35, s[14:15] offset:208
	global_load_dwordx4 v[26:29], v35, s[14:15] offset:192
	global_load_dwordx4 v[98:101], v35, s[14:15] offset:256
	global_load_dwordx4 v[102:105], v35, s[14:15] offset:272
	global_load_dwordx4 v[106:109], v35, s[14:15] offset:320
	global_load_dwordx4 v[110:113], v35, s[14:15] offset:336
	s_mov_b32 s0, 0xf800000
	s_waitcnt vmcnt(18)
	v_and_b32_e32 v58, 0xffff0000, v38
	v_lshlrev_b32_e32 v35, 16, v38
	v_mul_f32_e32 v89, v58, v58
	v_lshlrev_b32_e32 v60, 16, v39
	v_fmac_f32_e32 v89, v35, v35
	v_and_b32_e32 v62, 0xffff0000, v39
	v_fmac_f32_e32 v89, v60, v60
	v_lshlrev_b32_e32 v59, 16, v40
	v_fmac_f32_e32 v89, v62, v62
	v_and_b32_e32 v61, 0xffff0000, v40
	v_fmac_f32_e32 v89, v59, v59
	v_lshlrev_b32_e32 v63, 16, v41
	v_fmac_f32_e32 v89, v61, v61
	v_and_b32_e32 v64, 0xffff0000, v41
	v_fmac_f32_e32 v89, v63, v63
	s_waitcnt vmcnt(17)
	v_lshlrev_b32_e32 v65, 16, v42
	v_fmac_f32_e32 v89, v64, v64
	v_and_b32_e32 v66, 0xffff0000, v42
	v_fmac_f32_e32 v89, v65, v65
	v_lshlrev_b32_e32 v68, 16, v43
	v_fmac_f32_e32 v89, v66, v66
	v_and_b32_e32 v70, 0xffff0000, v43
	v_fmac_f32_e32 v89, v68, v68
	v_lshlrev_b32_e32 v67, 16, v44
	v_fmac_f32_e32 v89, v70, v70
	v_and_b32_e32 v69, 0xffff0000, v44
	v_fmac_f32_e32 v89, v67, v67
	v_lshlrev_b32_e32 v71, 16, v45
	v_fmac_f32_e32 v89, v69, v69
	v_and_b32_e32 v72, 0xffff0000, v45
	v_fmac_f32_e32 v89, v71, v71
	s_waitcnt vmcnt(16)
; __device__ __forceinline__ float half_pair_sum(float v) { const unsigned a = __float_as_uint(v); auto rr = __builtin_amdgcn_permlane32_swap(a, a, false, false); const unsigned r0 = rr[0], r1 = rr[1]; return __uint_as_float(r0) + __uint_as_float(r1); }
;   __device__ __forceinline__ void load(bf16x8 (&qr)[6], int r, int hi) const {
;     const bf16* src = qpre + (long)r * 1536 + hi * 8; float v[6][8]; float ss = 0.f;
; #pragma unroll
;     for (int d0 = 0; d0 < 6; ++d0) { unpack_bf8(*reinterpret_cast<const bf16x8*>(src + d0 * 16), v[d0]);
; #pragma unroll
;       for (int j = 0; j < 8; ++j) ss += v[d0][j] * v[d0][j]; }
;     ss = half_pair_sum(ss);
;     const float rqv = rq[r], f = Sc<96>::C * rqv / sqrtf(rqv * rqv * ss * (1.0f / 96.0f) + EPS);
; #pragma unroll
;     for (int d0 = 0; d0 < 6; ++d0) { const f32x4 g0 = *(const f32x4*)(gq + d0 * 16 + hi * 8), g1 = *(const f32x4*)(gq + d0 * 16 + hi * 8 + 4);
; #pragma unroll
;       for (int j = 0; j < 4; ++j) { v[d0][j] *= f * g0[j]; v[d0][4 + j] *= f * g1[j]; } }
;     if (cosA) { const float* c = cosA + (long)r * 16 + hi * 8; const float* sn = c + 4096 * 16;
; #pragma unroll
;       for (int j = 0; j < 8; ++j) { const float x1 = v[4][j], x2 = v[5][j], cs = c[j], si = sn[j]; v[4][j] = x1 * cs - x2 * si; v[5][j] = x1 * si + x2 * cs; } }
	v_lshlrev_b32_e32 v73, 16, v46
	v_fmac_f32_e32 v89, v72, v72
	v_and_b32_e32 v74, 0xffff0000, v46
	v_fmac_f32_e32 v89, v73, v73
	v_lshlrev_b32_e32 v76, 16, v47
	v_fmac_f32_e32 v89, v74, v74
	v_and_b32_e32 v78, 0xffff0000, v47
	v_fmac_f32_e32 v89, v76, v76
	v_lshlrev_b32_e32 v75, 16, v48
	v_fmac_f32_e32 v89, v78, v78
	v_and_b32_e32 v77, 0xffff0000, v48
	v_fmac_f32_e32 v89, v75, v75
	v_lshlrev_b32_e32 v79, 16, v49
	v_fmac_f32_e32 v89, v77, v77
	v_and_b32_e32 v80, 0xffff0000, v49
	v_fmac_f32_e32 v89, v79, v79
	s_waitcnt vmcnt(15)
	v_lshlrev_b32_e32 v81, 16, v50
	v_fmac_f32_e32 v89, v80, v80
	v_and_b32_e32 v82, 0xffff0000, v50
	v_fmac_f32_e32 v89, v81, v81
	v_lshlrev_b32_e32 v84, 16, v51
	v_fmac_f32_e32 v89, v82, v82
	v_and_b32_e32 v86, 0xffff0000, v51
	v_fmac_f32_e32 v89, v84, v84
	v_lshlrev_b32_e32 v83, 16, v52
	v_fmac_f32_e32 v89, v86, v86
	v_and_b32_e32 v85, 0xffff0000, v52
	v_fmac_f32_e32 v89, v83, v83
	v_lshlrev_b32_e32 v87, 16, v53
	v_fmac_f32_e32 v89, v85, v85
	v_and_b32_e32 v88, 0xffff0000, v53
	s_waitcnt vmcnt(13)
	v_and_b32_e32 v47, 0xffff0000, v90
	v_lshlrev_b32_e32 v46, 16, v90
	v_fmac_f32_e32 v89, v87, v87
	v_fmac_f32_e32 v89, v88, v88
	v_pk_mul_f32 v[118:119], v[46:47], v[46:47]
	v_and_b32_e32 v45, 0xffff0000, v91
	v_lshlrev_b32_e32 v44, 16, v91
	v_add_f32_e32 v89, v118, v89
	v_pk_mul_f32 v[114:115], v[44:45], v[44:45]
	v_add_f32_e32 v89, v119, v89
	v_and_b32_e32 v41, 0xffff0000, v92
	v_lshlrev_b32_e32 v40, 16, v92
	v_add_f32_e32 v89, v114, v89
	v_pk_mul_f32 v[90:91], v[40:41], v[40:41]
	v_add_f32_e32 v89, v115, v89
	v_and_b32_e32 v39, 0xffff0000, v93
	v_lshlrev_b32_e32 v38, 16, v93
	v_add_f32_e32 v89, v90, v89
	v_pk_mul_f32 v[50:51], v[38:39], v[38:39]
	v_add_f32_e32 v89, v91, v89
	s_waitcnt vmcnt(12)
	v_and_b32_e32 v93, 0xffff0000, v95
	v_lshlrev_b32_e32 v92, 16, v95
	v_and_b32_e32 v95, 0xffff0000, v94
	v_lshlrev_b32_e32 v94, 16, v94
	v_add_f32_e32 v50, v50, v89
	v_pk_mul_f32 v[118:119], v[94:95], v[94:95]
	v_add_f32_e32 v50, v51, v50
	v_add_f32_e32 v50, v118, v50
	v_pk_mul_f32 v[116:117], v[92:93], v[92:93]
	v_add_f32_e32 v50, v119, v50
	v_and_b32_e32 v49, 0xffff0000, v96
	v_lshlrev_b32_e32 v48, 16, v96
	v_add_f32_e32 v50, v116, v50
	v_and_b32_e32 v43, 0xffff0000, v97
	v_lshlrev_b32_e32 v42, 16, v97
	v_pk_mul_f32 v[96:97], v[48:49], v[48:49]
	v_add_f32_e32 v50, v117, v50
	v_add_f32_e32 v50, v96, v50
	v_pk_mul_f32 v[52:53], v[42:43], v[42:43]
	v_add_f32_e32 v50, v97, v50
	v_add_f32_e32 v50, v52, v50
	v_add_f32_e32 v50, v53, v50
	v_mov_b32_e32 v51, v50
	s_nop 1
	v_permlane32_swap_b32_e32 v50, v51
	v_mul_f32_e32 v54, v0, v0
	v_add_f32_e32 v50, v50, v51
	v_mul_f32_e32 v50, v54, v50
	v_fmamk_f32 v50, v50, 0x3c2aaaab, v250
	v_mul_f32_e32 v51, 0x4f800000, v50
	v_cmp_gt_f32_e32 vcc, s0, v50
	v_mul_f32_e32 v0, 0x3e16c740, v0
	s_nop 0
	v_cndmask_b32_e32 v50, v50, v51, vcc
	v_sqrt_f32_e32 v51, v50
	s_nop 0
	v_add_u32_e32 v52, -1, v51
	v_fma_f32 v53, -v52, v51, v50
	v_cmp_ge_f32_e64 s[0:1], 0, v53
	v_add_u32_e32 v53, 1, v51
	s_nop 0
	v_cndmask_b32_e64 v52, v51, v52, s[0:1]
	v_fma_f32 v51, -v53, v51, v50
	v_cmp_lt_f32_e64 s[0:1], 0, v51
	s_nop 1
	v_cndmask_b32_e64 v51, v52, v53, s[0:1]
	v_mul_f32_e32 v52, 0x37800000, v51
	v_cndmask_b32_e32 v51, v51, v52, vcc
	v_cmp_class_f32_e32 vcc, v50, v146
	s_nop 1
	v_cndmask_b32_e32 v50, v51, v50, vcc
	v_div_scale_f32 v51, s[0:1], v50, v50, v0
	v_rcp_f32_e32 v52, v51
	s_nop 0
	v_fma_f32 v53, -v51, v52, 1.0
	v_fmac_f32_e32 v52, v53, v52
	v_div_scale_f32 v53, vcc, v0, v50, v0
	v_mul_f32_e32 v54, v53, v52
	v_fma_f32 v89, -v51, v54, v53
	v_fmac_f32_e32 v54, v89, v52
	v_fma_f32 v51, -v51, v54, v53
	v_div_fmas_f32 v51, v51, v52, v54
	v_div_fixup_f32 v54, v51, v50, v0
	s_waitcnt vmcnt(3)
	v_pk_mul_f32 v[50:51], v[54:55], v[98:99] op_sel_hi:[0,1]
	s_waitcnt vmcnt(2)
	v_pk_mul_f32 v[52:53], v[54:55], v[102:103] op_sel_hi:[0,1]
	v_pk_mul_f32 v[50:51], v[50:51], v[46:47]
	v_pk_mul_f32 v[46:47], v[54:55], v[100:101] op_sel_hi:[0,1]
	v_pk_mul_f32 v[90:91], v[54:55], v[104:105] op_sel_hi:[0,1]
	v_pk_mul_f32 v[40:41], v[52:53], v[40:41]
	v_pk_mul_f32 v[52:53], v[46:47], v[44:45]
	v_pk_mul_f32 v[46:47], v[90:91], v[38:39]
	s_waitcnt vmcnt(1)
	v_pk_mul_f32 v[38:39], v[54:55], v[106:107] op_sel_hi:[0,1]
	s_waitcnt vmcnt(0)
	v_pk_mul_f32 v[90:91], v[54:55], v[110:111] op_sel_hi:[0,1]
	v_pk_mul_f32 v[44:45], v[38:39], v[94:95]
	v_pk_mul_f32 v[38:39], v[90:91], v[48:49]
	v_pk_mul_f32 v[48:49], v[54:55], v[108:109] op_sel_hi:[0,1]
	v_pk_mul_f32 v[90:91], v[54:55], v[112:113] op_sel_hi:[0,1]
	v_pk_mul_f32 v[48:49], v[48:49], v[92:93]
	s_and_b64 vcc, exec, s[36:37]
	v_pk_mul_f32 v[42:43], v[90:91], v[42:43]
	s_cbranch_vccnz .LBB0_1415
	v_lshlrev_b32_e32 v0, 3, v57
	v_lshlrev_b64 v[36:37], 6, v[36:37]
	v_lshl_add_u64 v[36:37], s[24:25], 0, v[36:37]
	v_lshlrev_b32_e32 v0, 2, v0
	v_lshl_add_u64 v[36:37], v[36:37], 0, v[0:1]
	s_mov_b64 s[0:1], 0x40000
	v_lshl_add_u64 v[102:103], v[36:37], 0, s[0:1]
	global_load_dwordx4 v[90:93], v[36:37], off offset:16
	global_load_dwordx4 v[94:97], v[36:37], off
	v_add_co_u32_e32 v36, vcc, 0x40000, v36
	s_nop 1
	v_addc_co_u32_e32 v37, vcc, 0, v37, vcc
	global_load_dwordx4 v[98:101], v[36:37], off
	s_nop 0
	global_load_dwordx4 v[102:105], v[102:103], off offset:16
	s_waitcnt vmcnt(1)
	v_pk_mul_f32 v[36:37], v[50:51], v[98:99]
	v_pk_mul_f32 v[98:99], v[44:45], v[98:99]
	v_pk_fma_f32 v[44:45], v[44:45], v[94:95], v[36:37]
	v_pk_fma_f32 v[50:51], v[50:51], v[94:95], v[98:99] neg_lo:[0,0,1] neg_hi:[0,0,1]
	v_pk_mul_f32 v[36:37], v[52:53], v[100:101]
	v_pk_mul_f32 v[94:95], v[48:49], v[100:101]
	v_pk_fma_f32 v[48:49], v[48:49], v[96:97], v[36:37]
	v_pk_fma_f32 v[52:53], v[52:53], v[96:97], v[94:95] neg_lo:[0,0,1] neg_hi:[0,0,1]
	s_waitcnt vmcnt(0)
	v_pk_mul_f32 v[36:37], v[40:41], v[102:103]
	v_pk_mul_f32 v[94:95], v[38:39], v[102:103]
	v_pk_fma_f32 v[38:39], v[38:39], v[90:91], v[36:37]
	v_pk_fma_f32 v[40:41], v[40:41], v[90:91], v[94:95] neg_lo:[0,0,1] neg_hi:[0,0,1]
	v_pk_mul_f32 v[36:37], v[46:47], v[104:105]
	v_pk_mul_f32 v[90:91], v[42:43], v[104:105]
	v_pk_fma_f32 v[42:43], v[42:43], v[92:93], v[36:37]
	v_pk_fma_f32 v[46:47], v[46:47], v[92:93], v[90:91] neg_lo:[0,0,1] neg_hi:[0,0,1]
; __device__ __forceinline__ bf16x8 pack_bf8(const float* f) { u32x4 w = {cvtpk(f[0], f[1]), cvtpk(f[2], f[3]), cvtpk(f[4], f[5]), cvtpk(f[6], f[7])}; return *reinterpret_cast<bf16x8*>(&w); }
;   __device__ __forceinline__ void load(bf16x8 (&qr)[6], int r, int hi) const {
;     ...
;     for (int d0 = 0; d0 < 6; ++d0) { const f32x4 g0 = *(const f32x4*)(gq + d0 * 16 + hi * 8), g1 = *(const f32x4*)(gq + d0 * 16 + hi * 8 + 4);
; #pragma unroll
;       for (int j = 0; j < 4; ++j) { v[d0][j] *= f * g0[j]; v[d0][4 + j] *= f * g1[j]; } }
;     if (cosA) { const float* c = cosA + (long)r * 16 + hi * 8; const float* sn = c + 4096 * 16;
; #pragma unroll
;       for (int j = 0; j < 8; ++j) { const float x1 = v[4][j], x2 = v[5][j], cs = c[j], si = sn[j]; v[4][j] = x1 * cs - x2 * si; v[5][j] = x1 * si + x2 * cs; } }
; #pragma unroll
;     for (int d0 = 0; d0 < 6; ++d0) qr[d0] = pack_bf8(v[d0]);
; template <int DK, int DV, bool OFF, class QLoader> ...
;     ...
;   for (int i = 0; i < (DK == 64 ? 1 : KPW); ++i) { const int row = (wid * KPW + i) * 4 + (lane >> 4); int c = (lane & 15) ^ (row & 7); c = (c < DK / 8) ? c : (c & 7); koff[i] = (unsigned)((row * ldk) * 2 + c * 16); }
; #pragma unroll
;   for (int i = 0; i < 1; ++i) { const int sidx = (wid * VPW + i) * 2 + (lane >> 5), kg = sidx / ND, st = sidx % ND, kk = kg * 8 + ((lane & 31) >> 2);
;     const int k = (kk & ~0xC) | ((kk & 4) << 1) | ((kk & 8) >> 1), c = st * 32 + (lane & 3) * 8; voff[i] = (unsigned)((k * ldv + c) * 2); }
.LBB0_1415:
	v_and_b32_e32 v36, 63, v56
	v_mul_f32_e32 v0, v54, v33
	v_mul_f32_e32 v3, v3, v54
	v_mul_f32_e32 v0, v0, v88
	v_mul_f32_e32 v29, v54, v29
	v_mul_f32_e32 v32, v54, v32
	v_mul_f32_e32 v28, v54, v28
	v_mul_f32_e32 v31, v54, v31
	v_mul_f32_e32 v27, v54, v27
	v_mul_f32_e32 v30, v54, v30
	v_mul_f32_e32 v26, v54, v26
	v_mul_f32_e32 v25, v54, v25
	v_mul_f32_e32 v21, v21, v54
	v_mul_f32_e32 v24, v54, v24
	v_mul_f32_e32 v20, v20, v54
	v_mul_f32_e32 v23, v54, v23
	v_mul_f32_e32 v19, v19, v54
	v_mul_f32_e32 v22, v54, v22
	v_mul_f32_e32 v18, v18, v54
	v_mul_f32_e32 v17, v17, v54
	v_mul_f32_e32 v13, v13, v54
	v_mul_f32_e32 v16, v16, v54
	v_mul_f32_e32 v12, v12, v54
	v_mul_f32_e32 v15, v15, v54
	v_mul_f32_e32 v11, v11, v54
	v_mul_f32_e32 v14, v14, v54
	v_mul_f32_e32 v10, v10, v54
	v_mul_f32_e32 v9, v9, v54
	v_mul_f32_e32 v5, v5, v54
	v_mul_f32_e32 v8, v8, v54
	v_mul_f32_e32 v4, v4, v54
	v_mul_f32_e32 v7, v7, v54
	v_mul_f32_e32 v3, v3, v58
	v_mul_f32_e32 v6, v6, v54
	v_mul_f32_e32 v2, v2, v54
	v_lshrrev_b32_e32 v149, 4, v36
	v_mul_f32_e32 v29, v29, v86
	v_mul_f32_e32 v32, v32, v87
	v_mul_f32_e32 v28, v28, v84
	v_mul_f32_e32 v31, v31, v85
	v_mul_f32_e32 v27, v27, v82
	v_mul_f32_e32 v30, v30, v83
	v_mul_f32_e32 v26, v26, v81
	v_mul_f32_e32 v25, v25, v80
	v_mul_f32_e32 v21, v21, v78
	v_mul_f32_e32 v24, v24, v79
	v_mul_f32_e32 v20, v20, v76
	v_mul_f32_e32 v23, v23, v77
	v_mul_f32_e32 v19, v19, v74
	v_mul_f32_e32 v22, v22, v75
	v_mul_f32_e32 v18, v18, v73
	v_mul_f32_e32 v17, v17, v72
	v_mul_f32_e32 v13, v13, v70
	v_mul_f32_e32 v16, v16, v71
	v_mul_f32_e32 v12, v12, v68
	v_mul_f32_e32 v15, v15, v69
	v_mul_f32_e32 v11, v11, v66
	v_mul_f32_e32 v14, v14, v67
	v_mul_f32_e32 v10, v10, v65
	v_mul_f32_e32 v9, v9, v64
	v_mul_f32_e32 v5, v5, v62
	v_mul_f32_e32 v8, v8, v63
	v_mul_f32_e32 v4, v4, v60
	v_mul_f32_e32 v7, v7, v61
	v_mul_f32_e32 v6, v6, v59
	v_mul_f32_e32 v2, v2, v35
	v_cvt_pk_bf16_f32 v98, v2, v3
	v_cvt_pk_bf16_f32 v99, v4, v5
	v_cvt_pk_bf16_f32 v100, v6, v7
	v_cvt_pk_bf16_f32 v101, v8, v9
	v_cvt_pk_bf16_f32 v102, v10, v11
	v_cvt_pk_bf16_f32 v103, v12, v13
	v_cvt_pk_bf16_f32 v104, v14, v15
	v_cvt_pk_bf16_f32 v105, v16, v17
	v_cvt_pk_bf16_f32 v106, v18, v19
	v_cvt_pk_bf16_f32 v107, v20, v21
	v_cvt_pk_bf16_f32 v108, v22, v23
	v_cvt_pk_bf16_f32 v109, v24, v25
	v_cvt_pk_bf16_f32 v110, v26, v27
	v_cvt_pk_bf16_f32 v111, v28, v29
	v_cvt_pk_bf16_f32 v112, v30, v31
	v_cvt_pk_bf16_f32 v113, v32, v0
	v_lshl_or_b32 v0, s38, 3, v149
	v_bitop3_b32 v3, v149, v56, 15 bitop3:0x78
	s_and_b32 s39, s38, 1
	s_lshl_b32 s39, s39, 3
	v_xor_b32_e32 v3, s39, v3
	s_movk_i32 s0, 0xc0
	v_and_b32_e32 v2, 15, v56
	v_mul_lo_u32 v4, v0, s0
	v_lshlrev_b32_e32 v0, 4, v3
	v_and_b32_e32 v3, 0x70, v0
	v_cmp_gt_u32_e32 vcc, 0xc0, v0
	v_bitop3_b32 v2, v149, v2, 4 bitop3:0x36
	v_xor_b32_e32 v2, s39, v2
	v_lshl_or_b32 v153, s38, 1, v57
	v_cndmask_b32_e32 v151, v3, v0, vcc
	v_lshlrev_b32_e32 v3, 4, v2
	v_cmp_gt_u32_e32 vcc, 12, v2
	v_lshrrev_b32_e32 v2, 31, v153
	v_and_b32_e32 v5, 0x70, v3
	v_add_u32_e32 v2, v153, v2
	v_cndmask_b32_e32 v150, v5, v3, vcc
	s_movk_i32 s0, 0x300
	v_ashrrev_i32_e32 v152, 1, v2
	v_add_u32_e32 v0, v151, v4
	v_add3_u32 v122, v4, v150, s0
	v_lshlrev_b32_e32 v3, 3, v152
	v_lshrrev_b32_e32 v4, 2, v55
	s_mov_b32 s0, 0x1fffff3
	v_bitop3_b32 v154, v3, s0, v4 bitop3:0xc8
	s_lshl_b32 s0, s38, 11
	v_lshrrev_b32_e32 v3, 1, v55
	s_add_i32 s87, s0, 0
	v_and_b32_e32 v2, 0x3fffffe, v2
	v_and_b32_e32 v155, 8, v3
	v_lshlrev_b32_e32 v3, 2, v152
	v_lshlrev_b32_e32 v4, 4, v56
	s_add_i32 s81, s87, 0x8000
	s_lshl_b32 s1, s38, 10
	v_cvt_pk_bf16_f32 v114, v50, v51
	v_cvt_pk_bf16_f32 v115, v52, v53
	v_cvt_pk_bf16_f32 v116, v40, v41
	v_cvt_pk_bf16_f32 v117, v46, v47
	v_cvt_pk_bf16_f32 v118, v44, v45
	v_cvt_pk_bf16_f32 v119, v48, v49
	v_cvt_pk_bf16_f32 v120, v38, v39
	v_cvt_pk_bf16_f32 v121, v42, v43
	s_waitcnt vmcnt(0)
	v_sub_u32_e32 v2, v153, v2
	v_and_b32_e32 v156, 4, v3
	v_and_b32_e32 v157, 48, v4
	s_sub_i32 s0, 0, s1
	s_sub_i32 s1, s87, s1
	s_mov_b32 m0, s81
	s_add_i32 s82, s87, 0x8400
	v_or3_b32 v3, v155, v154, v156
	v_lshl_or_b32 v2, v2, 6, v157
	s_mov_b32 m0, s82
	s_add_u32 s40, s20, 0x3000
	v_lshl_add_u32 v2, v3, 7, v2
	s_mov_b32 m0, s1
	s_addc_u32 s41, s21, 0
	s_add_i32 s83, s87, 0xc000
	s_mov_b32 m0, s83
	s_add_i32 s84, s87, 0xc400
	v_mov_b32_e32 v3, v1
	s_mov_b32 m0, s84
	v_lshl_add_u64 v[124:125], s[22:23], 0, v[2:3]
	s_mov_b64 s[40:41], 0x2000
	s_add_i32 m0, s1, 0x2000
	v_lshl_add_u64 v[2:3], v[124:125], 0, s[40:41]
	s_add_u32 s40, s20, 0x6000
	s_addc_u32 s41, s21, 0
	s_add_i32 m0, s87, 0x10000
	s_waitcnt vmcnt(3)
	s_waitcnt vmcnt(0) lgkmcnt(0)
	s_barrier
; #define DMA_WAIT(last) do { if (last) asm volatile("s_waitcnt vmcnt(0)" ::: "memory"); else asm volatile("s_waitcnt vmcnt(%0)" :: "n"(NPW) : "memory"); } while (0)
; template <int DK>
; __device__ __forceinline__ void qkt(f32x16& p0, f32x16& p1, const char* Ks, const bf16x8* qr, int r32, int hi) {
;   p0 = f32x16{}; p1 = f32x16{};
; #pragma unroll
;   for (int d0 = 0; d0 < DK / 16; ++d0) { const int cb = (d0 * 16 + hi * 8) * 2;
;     const bf16x8 b0 = *reinterpret_cast<const bf16x8*>(Ks + ATT_KSWZ(r32, cb));
;     const bf16x8 b1 = *reinterpret_cast<const bf16x8*>(Ks + ATT_KSWZ(32 + r32, cb));
;     p0 = __builtin_amdgcn_mfma_f32_32x32x16_bf16(b0, qr[d0], p0, 0, 0, 0);
;     p1 = __builtin_amdgcn_mfma_f32_32x32x16_bf16(b1, qr[d0], p1, 0, 0, 0);
;   }
; template <int DK, int DV, bool OFF, class QLoader> ...
;     ...
;   f32x16 pA0, pA1, pB0, pB1; bf16x8 pa0, pa1, pa2, pa3; const int NT = nkeys / KVBLK;
;   DMA_TILE(0, 0); DMA_TILE(1, 1); DMA_WAIT(false); __syncthreads(); if (2 < NT) DMA_TILE(2, 2);
;   qkt<DK>(pA0, pA1, K_lds, qr, r32, hi); partialSM<DK, OFF>(pA0, pA1, negMC);
	global_load_lds_dwordx4 v0, s[40:41]
	s_add_i32 m0, s87, 0x10400
	v_lshlrev_b32_e32 v35, 8, v55
	global_load_lds_dwordx4 v122, s[40:41]
	s_mov_b64 s[40:41], 0x4000
	v_lshl_add_u64 v[2:3], v[124:125], 0, s[40:41]
	s_add_i32 m0, s1, 0x4000
	v_or_b32_e32 v38, 32, v34
	global_load_lds_dwordx4 v[2:3], off
	v_lshlrev_b32_e32 v2, 4, v55
	v_and_b32_e32 v37, 0xf0, v2
	v_bitop3_b32 v140, v34, v35, v37 bitop3:0xde
	v_add_u32_e32 v126, 0, v140
	ds_read_b128 v[2:5], v126 offset:32768
	v_bitop3_b32 v141, v38, v35, v37 bitop3:0xde
	v_add_u32_e32 v127, 0, v141
	ds_read_b128 v[38:41], v127 offset:32768
	s_waitcnt lgkmcnt(0)
	v_mfma_f32_32x32x16_bf16 v[18:33], v[2:5], v[98:101], 0
	ds_read_b128 v[2:5], v126 offset:40960
	s_cmp_lt_i32 s38, 4
	v_mfma_f32_32x32x16_bf16 v[18:33], v[38:41], v[102:105], v[18:33]
	ds_read_b128 v[38:41], v127 offset:40960
	s_waitcnt lgkmcnt(0)
	v_mfma_f32_32x32x16_bf16 v[2:17], v[2:5], v[98:101], 0
	v_mfma_f32_32x32x16_bf16 v[2:17], v[38:41], v[102:105], v[2:17]
	v_or_b32_e32 v38, 64, v34
	v_bitop3_b32 v142, v38, v35, v37 bitop3:0xde
	v_add_u32_e32 v128, 0, v142
	ds_read_b128 v[38:41], v128 offset:32768
	s_waitcnt lgkmcnt(0)
	v_mfma_f32_32x32x16_bf16 v[18:33], v[38:41], v[106:109], v[18:33]
	ds_read_b128 v[38:41], v128 offset:40960
	s_waitcnt lgkmcnt(0)
	v_mfma_f32_32x32x16_bf16 v[2:17], v[38:41], v[106:109], v[2:17]
	v_or_b32_e32 v38, 0x60, v34
	v_bitop3_b32 v143, v38, v35, v37 bitop3:0xde
	v_add_u32_e32 v129, 0, v143
	ds_read_b128 v[38:41], v129 offset:32768
	s_waitcnt lgkmcnt(0)
	v_mfma_f32_32x32x16_bf16 v[18:33], v[38:41], v[110:113], v[18:33]
	ds_read_b128 v[38:41], v129 offset:40960
	s_waitcnt lgkmcnt(0)
	v_mfma_f32_32x32x16_bf16 v[2:17], v[38:41], v[110:113], v[2:17]
	v_or_b32_e32 v38, 0x80, v34
	v_bitop3_b32 v144, v38, v35, v37 bitop3:0xde
	v_add_u32_e32 v130, 0, v144
	ds_read_b128 v[38:41], v130 offset:32768
	v_or_b32_e32 v34, 0xa0, v34
	v_bitop3_b32 v145, v34, v35, v37 bitop3:0xde
	v_add_u32_e32 v131, 0, v145
	s_waitcnt lgkmcnt(0)
	v_mfma_f32_32x32x16_bf16 v[18:33], v[38:41], v[114:117], v[18:33]
	ds_read_b128 v[38:41], v130 offset:40960
	s_waitcnt lgkmcnt(0)
	v_mfma_f32_32x32x16_bf16 v[2:17], v[38:41], v[114:117], v[2:17]
	ds_read_b128 v[38:41], v131 offset:32768
	s_waitcnt lgkmcnt(0)
	v_mfma_f32_32x32x16_bf16 v[18:33], v[38:41], v[118:121], v[18:33]
	ds_read_b128 v[38:41], v131 offset:40960
	s_waitcnt lgkmcnt(0)
	v_mfma_f32_32x32x16_bf16 v[2:17], v[38:41], v[118:121], v[2:17]
	s_cbranch_scc1 .LBB0_1417
	s_setprio 1
